# attention unit epilogue combine: LDS reads issued eight at a time into dead registers with counted lgkmcnt(7) instead of 32 serialized read-wait-compute-write round trips
# baseline (speedup 1.0000x reference)
.LBB0_1076:
	s_andn2_b64 vcc, exec, s[4:5]
	s_waitcnt lgkmcnt(0)
	s_barrier
	s_cbranch_vccnz .LBB0_1020
	v_add_u32_e32 v86, 0x400, v68
	v_add_u32_e32 v87, 0x1000, v68
	v_add_u32_e32 v88, 0x1400, v68
	v_add_u32_e32 v89, 0x2000, v68
	v_add_u32_e32 v90, 0x2400, v68
	v_add_u32_e32 v91, 0x3000, v68
	v_add_u32_e32 v92, 0x3400, v68
	ds_read2_b32 v[100:101], v68 offset1:32
	ds_read2_b32 v[102:103], v68 offset0:64 offset1:96
	ds_read2_b32 v[104:105], v68 offset0:128 offset1:160
	ds_read2_b32 v[106:107], v68 offset0:192 offset1:224
	ds_read2_b32 v[108:109], v86 offset1:32
	ds_read2_b32 v[110:111], v86 offset0:64 offset1:96
	ds_read2_b32 v[112:113], v86 offset0:128 offset1:160
	ds_read2_b32 v[114:115], v86 offset0:192 offset1:224
	s_lshl_b64 s[4:5], s[90:91], 11
	s_add_u32 s4, s95, s4
	s_addc_u32 s5, s96, s5
	s_add_u32 s4, s4, s29
	s_waitcnt lgkmcnt(7)
	v_mul_f32_e32 v83, v239, v100
	v_fma_f32 v2, v2, v82, -v83
	v_mul_f32_e32 v83, v239, v101
	v_fma_f32 v50, v50, v82, -v83
	ds_write2_b32 v68, v2, v50 offset1:32
	s_addc_u32 s5, s5, 0
	s_add_u32 s6, s92, s84
	s_waitcnt lgkmcnt(7)
	v_mul_f32_e32 v2, v239, v102
	v_fma_f32 v2, v34, v82, -v2
	v_mul_f32_e32 v34, v239, v103
	v_fma_f32 v18, v18, v82, -v34
	ds_write2_b32 v68, v2, v18 offset0:64 offset1:96
	s_addc_u32 s7, s93, s85
	v_mov_b32_e32 v211, v1
	s_waitcnt lgkmcnt(7)
	v_mul_f32_e32 v2, v239, v104
	v_fma_f32 v2, v3, v81, -v2
	v_mul_f32_e32 v3, v239, v105
	v_fma_f32 v3, v51, v81, -v3
	ds_write2_b32 v68, v2, v3 offset0:128 offset1:160
	v_mov_b32_e32 v213, v1
	s_waitcnt lgkmcnt(7)
	v_mul_f32_e32 v2, v239, v106
	v_mul_f32_e32 v3, v239, v107
	v_fma_f32 v2, v35, v81, -v2
	v_fma_f32 v3, v19, v81, -v3
	ds_write2_b32 v68, v2, v3 offset0:192 offset1:224
	s_waitcnt lgkmcnt(7)
	v_mul_f32_e32 v2, v239, v108
	v_mul_f32_e32 v3, v239, v109
	v_fma_f32 v2, v4, v80, -v2
	v_fma_f32 v3, v52, v80, -v3
	ds_write2_b32 v86, v2, v3 offset1:32
	s_waitcnt lgkmcnt(7)
	v_mul_f32_e32 v2, v239, v110
	v_mul_f32_e32 v3, v239, v111
	v_fma_f32 v2, v36, v80, -v2
	v_fma_f32 v3, v20, v80, -v3
	ds_write2_b32 v86, v2, v3 offset0:64 offset1:96
	s_waitcnt lgkmcnt(7)
	v_mul_f32_e32 v2, v239, v112
	v_mul_f32_e32 v3, v239, v113
	v_fma_f32 v2, v5, v79, -v2
	v_fma_f32 v3, v53, v79, -v3
	ds_write2_b32 v86, v2, v3 offset0:128 offset1:160
	s_waitcnt lgkmcnt(7)
	v_mul_f32_e32 v2, v239, v114
	v_mul_f32_e32 v3, v239, v115
	v_fma_f32 v2, v37, v79, -v2
	v_fma_f32 v3, v21, v79, -v3
	ds_write2_b32 v86, v2, v3 offset0:192 offset1:224
	ds_read2_b32 v[100:101], v87 offset1:32
	ds_read2_b32 v[102:103], v87 offset0:64 offset1:96
	ds_read2_b32 v[104:105], v87 offset0:128 offset1:160
	ds_read2_b32 v[106:107], v87 offset0:192 offset1:224
	ds_read2_b32 v[108:109], v88 offset1:32
	ds_read2_b32 v[110:111], v88 offset0:64 offset1:96
	ds_read2_b32 v[112:113], v88 offset0:128 offset1:160
	ds_read2_b32 v[114:115], v88 offset0:192 offset1:224
	s_waitcnt lgkmcnt(7)
	v_mul_f32_e32 v2, v239, v100
	v_mul_f32_e32 v3, v239, v101
	v_fma_f32 v2, v6, v78, -v2
	v_fma_f32 v3, v54, v78, -v3
	ds_write2_b32 v87, v2, v3 offset1:32
	s_waitcnt lgkmcnt(7)
	v_mul_f32_e32 v2, v239, v102
	v_mul_f32_e32 v3, v239, v103
	v_fma_f32 v2, v38, v78, -v2
	v_fma_f32 v3, v22, v78, -v3
	ds_write2_b32 v87, v2, v3 offset0:64 offset1:96
	s_waitcnt lgkmcnt(7)
	v_mul_f32_e32 v2, v239, v104
	v_mul_f32_e32 v3, v239, v105
	v_fma_f32 v2, v7, v77, -v2
	v_fma_f32 v3, v55, v77, -v3
	ds_write2_b32 v87, v2, v3 offset0:128 offset1:160
	s_waitcnt lgkmcnt(7)
	v_mul_f32_e32 v2, v239, v106
	v_mul_f32_e32 v3, v239, v107
	v_fma_f32 v2, v39, v77, -v2
	v_fma_f32 v3, v23, v77, -v3
	ds_write2_b32 v87, v2, v3 offset0:192 offset1:224
	s_waitcnt lgkmcnt(7)
	v_mul_f32_e32 v2, v239, v108
	v_mul_f32_e32 v3, v239, v109
	v_fma_f32 v2, v8, v76, -v2
	v_fma_f32 v3, v56, v76, -v3
	ds_write2_b32 v88, v2, v3 offset1:32
	s_waitcnt lgkmcnt(7)
	v_mul_f32_e32 v2, v239, v110
	v_mul_f32_e32 v3, v239, v111
	v_fma_f32 v2, v40, v76, -v2
	v_fma_f32 v3, v24, v76, -v3
	ds_write2_b32 v88, v2, v3 offset0:64 offset1:96
	s_waitcnt lgkmcnt(7)
	v_mul_f32_e32 v2, v239, v112
	v_mul_f32_e32 v3, v239, v113
	v_fma_f32 v2, v9, v75, -v2
	v_fma_f32 v3, v57, v75, -v3
	ds_write2_b32 v88, v2, v3 offset0:128 offset1:160
	s_waitcnt lgkmcnt(7)
	v_mul_f32_e32 v2, v239, v114
	v_mul_f32_e32 v3, v239, v115
	v_fma_f32 v2, v41, v75, -v2
	v_fma_f32 v3, v25, v75, -v3
	ds_write2_b32 v88, v2, v3 offset0:192 offset1:224
	ds_read2_b32 v[100:101], v89 offset1:32
	ds_read2_b32 v[102:103], v89 offset0:64 offset1:96
	ds_read2_b32 v[104:105], v89 offset0:128 offset1:160
	ds_read2_b32 v[106:107], v89 offset0:192 offset1:224
	ds_read2_b32 v[108:109], v90 offset1:32
	ds_read2_b32 v[110:111], v90 offset0:64 offset1:96
	ds_read2_b32 v[112:113], v90 offset0:128 offset1:160
	ds_read2_b32 v[114:115], v90 offset0:192 offset1:224
	s_waitcnt lgkmcnt(7)
	v_mul_f32_e32 v2, v239, v100
	v_mul_f32_e32 v3, v239, v101
	v_fma_f32 v2, v10, v74, -v2
	v_fma_f32 v3, v58, v74, -v3
	ds_write2_b32 v89, v2, v3 offset1:32
	v_lshlrev_b32_e32 v10, 2, v198
	s_waitcnt lgkmcnt(7)
	v_mul_f32_e32 v2, v239, v102
	v_mul_f32_e32 v3, v239, v103
	v_fma_f32 v2, v42, v74, -v2
	v_fma_f32 v3, v26, v74, -v3
	ds_write2_b32 v89, v2, v3 offset0:64 offset1:96
	s_waitcnt lgkmcnt(7)
	v_mul_f32_e32 v2, v239, v104
	v_mul_f32_e32 v3, v239, v105
	v_fma_f32 v2, v11, v73, -v2
	v_fma_f32 v3, v59, v73, -v3
	ds_write2_b32 v89, v2, v3 offset0:128 offset1:160
	v_mov_b32_e32 v11, v1
	s_waitcnt lgkmcnt(7)
	v_mul_f32_e32 v2, v239, v106
	v_mul_f32_e32 v3, v239, v107
	v_fma_f32 v2, v43, v73, -v2
	v_fma_f32 v3, v27, v73, -v3
	ds_write2_b32 v89, v2, v3 offset0:192 offset1:224
	s_waitcnt lgkmcnt(7)
	v_mul_f32_e32 v2, v239, v108
	v_mul_f32_e32 v3, v239, v109
	v_fma_f32 v2, v12, v72, -v2
	v_fma_f32 v3, v60, v72, -v3
	ds_write2_b32 v90, v2, v3 offset1:32
	s_waitcnt lgkmcnt(7)
	v_mul_f32_e32 v2, v239, v110
	v_mul_f32_e32 v3, v239, v111
	v_fma_f32 v2, v44, v72, -v2
	v_fma_f32 v3, v28, v72, -v3
	ds_write2_b32 v90, v2, v3 offset0:64 offset1:96
	s_waitcnt lgkmcnt(7)
	v_mul_f32_e32 v2, v239, v112
	v_mul_f32_e32 v3, v239, v113
	v_fma_f32 v2, v13, v71, -v2
	v_fma_f32 v3, v61, v71, -v3
	ds_write2_b32 v90, v2, v3 offset0:128 offset1:160
	s_waitcnt lgkmcnt(7)
	v_mul_f32_e32 v2, v239, v114
	v_mul_f32_e32 v3, v239, v115
	v_fma_f32 v2, v45, v71, -v2
	v_fma_f32 v3, v29, v71, -v3
	ds_write2_b32 v90, v2, v3 offset0:192 offset1:224
	ds_read2_b32 v[100:101], v91 offset1:32
	ds_read2_b32 v[102:103], v91 offset0:64 offset1:96
	ds_read2_b32 v[104:105], v91 offset0:128 offset1:160
	ds_read2_b32 v[106:107], v91 offset0:192 offset1:224
	ds_read2_b32 v[108:109], v92 offset1:32
	ds_read2_b32 v[110:111], v92 offset0:64 offset1:96
	ds_read2_b32 v[112:113], v92 offset0:128 offset1:160
	ds_read2_b32 v[114:115], v92 offset0:192 offset1:224
	s_waitcnt lgkmcnt(7)
	v_mul_f32_e32 v2, v239, v100
	v_mul_f32_e32 v3, v239, v101
	v_fma_f32 v2, v14, v70, -v2
	v_fma_f32 v3, v62, v70, -v3
	ds_write2_b32 v91, v2, v3 offset1:32
	v_add3_u32 v14, s8, v249, v10
	v_add_u32_e32 v25, v14, v210
	v_add_u32_e32 v24, v14, v212
	s_waitcnt lgkmcnt(7)
	v_mul_f32_e32 v2, v239, v102
	v_mul_f32_e32 v3, v239, v103
	v_fma_f32 v2, v46, v70, -v2
	v_fma_f32 v3, v30, v70, -v3
	ds_write2_b32 v91, v2, v3 offset0:64 offset1:96
	s_waitcnt lgkmcnt(7)
	v_mul_f32_e32 v2, v239, v104
	v_mul_f32_e32 v3, v239, v105
	v_fma_f32 v2, v15, v69, -v2
	v_fma_f32 v3, v63, v69, -v3
	ds_write2_b32 v91, v2, v3 offset0:128 offset1:160
	s_waitcnt lgkmcnt(7)
	v_mul_f32_e32 v2, v239, v106
	v_mul_f32_e32 v3, v239, v107
	v_fma_f32 v2, v47, v69, -v2
	v_fma_f32 v3, v31, v69, -v3
	ds_write2_b32 v91, v2, v3 offset0:192 offset1:224
	s_waitcnt lgkmcnt(7)
	v_mul_f32_e32 v2, v239, v108
	v_mul_f32_e32 v3, v239, v109
	v_fma_f32 v2, v16, v67, -v2
	v_fma_f32 v3, v64, v67, -v3
	ds_write2_b32 v92, v2, v3 offset1:32
	s_waitcnt lgkmcnt(7)
	v_mul_f32_e32 v2, v239, v110
	v_mul_f32_e32 v3, v239, v111
	v_fma_f32 v2, v48, v67, -v2
	v_fma_f32 v3, v32, v67, -v3
	ds_write2_b32 v92, v2, v3 offset0:64 offset1:96
	s_waitcnt lgkmcnt(7)
	v_mul_f32_e32 v2, v239, v112
	v_mul_f32_e32 v3, v239, v113
	v_fma_f32 v2, v17, v66, -v2
	v_fma_f32 v3, v65, v66, -v3
	ds_write2_b32 v92, v2, v3 offset0:128 offset1:160
	s_waitcnt lgkmcnt(7)
	v_mul_f32_e32 v2, v239, v114
	v_mul_f32_e32 v3, v239, v115
	v_fma_f32 v2, v49, v66, -v2
	v_fma_f32 v3, v33, v66, -v3
	ds_write2_b32 v92, v2, v3 offset0:192 offset1:224
	v_lshl_add_u64 v[2:3], s[6:7], 0, v[10:11]
	v_or_b32_e32 v10, s88, v241
	v_ashrrev_i32_e32 v11, 31, v10
	s_waitcnt lgkmcnt(0)
	v_lshl_add_u64 v[4:5], v[2:3], 0, v[210:211]
	v_lshlrev_b64 v[10:11], 11, v[10:11]
	global_load_dwordx4 v[6:9], v[4:5], off
	v_lshl_add_u64 v[10:11], s[4:5], 0, v[10:11]
	v_lshl_add_u64 v[18:19], v[10:11], 0, v[198:199]
	v_and_b32_e32 v11, 64, v226
	v_xor_b32_e32 v10, 1, v226
	v_add_u32_e32 v11, 64, v11
	v_cmp_lt_i32_e32 vcc, v10, v11
	v_lshl_add_u64 v[2:3], v[2:3], 0, v[212:213]
	global_load_dwordx4 v[2:5], v[2:3], off
	v_cndmask_b32_e32 v10, v226, v10, vcc
	v_lshlrev_b32_e32 v23, 2, v10
	v_xor_b32_e32 v10, 2, v226
	v_cmp_lt_i32_e32 vcc, v10, v11
	ds_read_b128 v[14:17], v24
	s_nop 0
	v_cndmask_b32_e32 v10, v226, v10, vcc
	v_lshlrev_b32_e32 v22, 2, v10
	v_xor_b32_e32 v10, 4, v226
	v_cmp_lt_i32_e32 vcc, v10, v11
	s_nop 1
	v_cndmask_b32_e32 v10, v226, v10, vcc
	v_lshlrev_b32_e32 v21, 2, v10
	v_xor_b32_e32 v10, 8, v226
	v_cmp_lt_i32_e32 vcc, v10, v11
	s_nop 1
	v_cndmask_b32_e32 v10, v226, v10, vcc
	v_lshlrev_b32_e32 v20, 2, v10
	ds_read_b128 v[10:13], v25
	s_waitcnt lgkmcnt(0)
	v_mul_f32_e32 v26, v11, v11
	v_mul_f32_e32 v27, v13, v13
	v_fmac_f32_e32 v26, v10, v10
	v_fmac_f32_e32 v27, v12, v12
	v_add_f32_e32 v26, v26, v27
	v_mul_f32_e32 v27, v15, v15
	v_fmac_f32_e32 v27, v14, v14
	v_add_f32_e32 v26, v26, v27
	v_mul_f32_e32 v27, v17, v17
	v_fmac_f32_e32 v27, v16, v16
	v_add_f32_e32 v26, v27, v26
	s_nop 1
	v_mov_b32_dpp v27, v26 quad_perm:[1,0,3,2] row_mask:0xf bank_mask:0xf
	s_waitcnt lgkmcnt(0)
	v_add_f32_e32 v26, v26, v27
	s_nop 1
	v_mov_b32_dpp v27, v26 quad_perm:[2,3,0,1] row_mask:0xf bank_mask:0xf
	s_waitcnt lgkmcnt(0)
	v_add_f32_e32 v26, v26, v27
	s_nop 1
	v_mov_b32_dpp v27, v26 row_half_mirror row_mask:0xf bank_mask:0xf
	s_waitcnt lgkmcnt(0)
	v_add_f32_e32 v26, v26, v27
	s_nop 1
	v_mov_b32_dpp v27, v26 row_mirror row_mask:0xf bank_mask:0xf
	s_waitcnt lgkmcnt(0)
	v_add_f32_e32 v26, v26, v27
	v_fmamk_f32 v26, v26, 0x3c000000, v232
	v_cmp_gt_f32_e32 vcc, s82, v26
	v_mul_f32_e32 v27, 0x4f800000, v26
	s_nop 0
	v_cndmask_b32_e32 v26, v26, v27, vcc
	v_sqrt_f32_e32 v27, v26
	s_nop 0
	v_add_u32_e32 v28, -1, v27
	v_fma_f32 v29, -v28, v27, v26
	v_cmp_ge_f32_e64 s[44:45], 0, v29
	v_add_u32_e32 v29, 1, v27
	s_nop 0
	v_cndmask_b32_e64 v28, v27, v28, s[44:45]
	v_fma_f32 v27, -v29, v27, v26
	v_cmp_lt_f32_e64 s[44:45], 0, v27
	s_nop 1
	v_cndmask_b32_e64 v27, v28, v29, s[44:45]
	v_mul_f32_e32 v28, 0x37800000, v27
	v_cndmask_b32_e32 v27, v27, v28, vcc
	v_cmp_class_f32_e32 vcc, v26, v229
	s_nop 1
	v_cndmask_b32_e32 v26, v27, v26, vcc
	v_div_scale_f32 v27, s[4:5], v26, v26, v237
	v_rcp_f32_e32 v28, v27
	s_nop 0
	v_fma_f32 v29, -v27, v28, 1.0
	v_fmac_f32_e32 v28, v29, v28
	v_div_scale_f32 v29, vcc, v237, v26, v237
	v_mul_f32_e32 v30, v29, v28
	v_fma_f32 v31, -v27, v30, v29
	v_fmac_f32_e32 v30, v31, v28
	v_fma_f32 v27, -v27, v30, v29
	v_div_fmas_f32 v27, v27, v28, v30
	v_div_fixup_f32 v26, v27, v26, v237
	v_mul_f32_e32 v10, v10, v26
	v_mul_f32_e32 v11, v11, v26
	s_waitcnt vmcnt(1)
	v_mul_f32_e32 v10, v6, v10
	v_mul_f32_e32 v11, v7, v11
	v_med3_f32 v10, v10, s33, v233
	v_med3_f32 v11, v11, s33, v233
	v_mov_b32_e32 v27, v1
	v_cvt_pk_fp8_f32 v27, v10, v11
	v_mul_f32_e32 v12, v12, v26
	v_mul_f32_e32 v13, v13, v26
	v_mul_f32_e32 v12, v8, v12
	v_mul_f32_e32 v13, v9, v13
	v_med3_f32 v10, v12, s33, v233
	v_med3_f32 v11, v13, s33, v233
	v_cvt_pk_fp8_f32 v27, v10, v11 op_sel:[0,0,1]
	v_mul_f32_e32 v10, v14, v26
	v_mul_f32_e32 v11, v15, v26
	s_waitcnt vmcnt(0)
	v_mul_f32_e32 v10, v2, v10
	v_mul_f32_e32 v11, v3, v11
	v_med3_f32 v10, v10, s33, v233
	v_med3_f32 v11, v11, s33, v233
	v_mov_b32_e32 v14, v1
	v_cvt_pk_fp8_f32 v14, v10, v11
	v_mul_f32_e32 v12, v16, v26
	v_mul_f32_e32 v13, v17, v26
	v_mul_f32_e32 v12, v4, v12
	v_mul_f32_e32 v13, v5, v13
	v_med3_f32 v10, v12, s33, v233
	v_med3_f32 v11, v13, s33, v233
	v_cvt_pk_fp8_f32 v14, v10, v11 op_sel:[0,0,1]
	s_nop 0
	v_cndmask_b32_e64 v10, v14, v27, s[42:43]
	v_cndmask_b32_e64 v11, v27, v14, s[42:43]
	global_store_dwordx2 v[18:19], v[10:11], off
	ds_read_b128 v[10:13], v25 offset:2048
	ds_read_b128 v[14:17], v24 offset:2048
	s_waitcnt lgkmcnt(1)
	v_mul_f32_e32 v26, v11, v11
	v_mul_f32_e32 v27, v13, v13
	v_fmac_f32_e32 v26, v10, v10
	v_fmac_f32_e32 v27, v12, v12
	v_add_f32_e32 v26, v26, v27
	s_waitcnt lgkmcnt(0)
	v_mul_f32_e32 v27, v15, v15
	v_fmac_f32_e32 v27, v14, v14
	v_add_f32_e32 v26, v26, v27
	v_mul_f32_e32 v27, v17, v17
	v_fmac_f32_e32 v27, v16, v16
	v_add_f32_e32 v26, v27, v26
	s_nop 1
	v_mov_b32_dpp v27, v26 quad_perm:[1,0,3,2] row_mask:0xf bank_mask:0xf
	s_waitcnt lgkmcnt(0)
	v_add_f32_e32 v26, v26, v27
	s_nop 1
	v_mov_b32_dpp v27, v26 quad_perm:[2,3,0,1] row_mask:0xf bank_mask:0xf
	s_waitcnt lgkmcnt(0)
	v_add_f32_e32 v26, v26, v27
	s_nop 1
	v_mov_b32_dpp v27, v26 row_half_mirror row_mask:0xf bank_mask:0xf
	s_waitcnt lgkmcnt(0)
	v_add_f32_e32 v26, v26, v27
	s_nop 1
	v_mov_b32_dpp v27, v26 row_mirror row_mask:0xf bank_mask:0xf
	s_waitcnt lgkmcnt(0)
	v_add_f32_e32 v26, v26, v27
	v_fmamk_f32 v26, v26, 0x3c000000, v232
	v_cmp_gt_f32_e32 vcc, s82, v26
	v_mul_f32_e32 v27, 0x4f800000, v26
	s_nop 0
	v_cndmask_b32_e32 v26, v26, v27, vcc
	v_sqrt_f32_e32 v27, v26
	s_nop 0
	v_add_u32_e32 v28, -1, v27
	v_fma_f32 v29, -v28, v27, v26
	v_cmp_ge_f32_e64 s[44:45], 0, v29
	v_add_u32_e32 v29, 1, v27
	s_nop 0
	v_cndmask_b32_e64 v28, v27, v28, s[44:45]
	v_fma_f32 v27, -v29, v27, v26
	v_cmp_lt_f32_e64 s[44:45], 0, v27
	s_nop 1
	v_cndmask_b32_e64 v27, v28, v29, s[44:45]
	v_mul_f32_e32 v28, 0x37800000, v27
	v_cndmask_b32_e32 v27, v27, v28, vcc
	v_cmp_class_f32_e32 vcc, v26, v229
	s_nop 1
	v_cndmask_b32_e32 v26, v27, v26, vcc
	v_div_scale_f32 v27, s[4:5], v26, v26, v237
	v_rcp_f32_e32 v28, v27
	s_movk_i32 s4, 0x2000
	v_fma_f32 v29, -v27, v28, 1.0
	v_fmac_f32_e32 v28, v29, v28
	v_div_scale_f32 v29, vcc, v237, v26, v237
	v_mul_f32_e32 v30, v29, v28
	v_fma_f32 v31, -v27, v30, v29
	v_fmac_f32_e32 v30, v31, v28
	v_fma_f32 v27, -v27, v30, v29
	v_div_fmas_f32 v27, v27, v28, v30
	v_div_fixup_f32 v26, v27, v26, v237
	v_mul_f32_e32 v10, v10, v26
	v_mul_f32_e32 v11, v11, v26
	v_mul_f32_e32 v10, v6, v10
	v_mul_f32_e32 v11, v7, v11
	v_med3_f32 v10, v10, s33, v233
	v_med3_f32 v11, v11, s33, v233
	v_mov_b32_e32 v27, v1
	v_cvt_pk_fp8_f32 v27, v10, v11
	v_mul_f32_e32 v12, v12, v26
	v_mul_f32_e32 v13, v13, v26
	v_mul_f32_e32 v12, v8, v12
	v_mul_f32_e32 v13, v9, v13
	v_med3_f32 v10, v12, s33, v233
	v_med3_f32 v11, v13, s33, v233
	v_cvt_pk_fp8_f32 v27, v10, v11 op_sel:[0,0,1]
	v_mul_f32_e32 v10, v14, v26
	v_mul_f32_e32 v11, v15, v26
	v_mul_f32_e32 v10, v2, v10
	v_mul_f32_e32 v11, v3, v11
	v_med3_f32 v10, v10, s33, v233
	v_med3_f32 v11, v11, s33, v233
	v_mov_b32_e32 v14, v1
	v_cvt_pk_fp8_f32 v14, v10, v11
	v_mul_f32_e32 v12, v16, v26
	v_mul_f32_e32 v13, v17, v26
	v_mul_f32_e32 v12, v4, v12
	v_mul_f32_e32 v13, v5, v13
	v_med3_f32 v10, v12, s33, v233
	v_med3_f32 v11, v13, s33, v233
	v_cvt_pk_fp8_f32 v14, v10, v11 op_sel:[0,0,1]
	v_add_co_u32_e32 v12, vcc, s4, v18
	v_cndmask_b32_e64 v10, v14, v27, s[42:43]
	v_cndmask_b32_e64 v11, v27, v14, s[42:43]
	v_addc_co_u32_e32 v13, vcc, 0, v19, vcc
	global_store_dwordx2 v[12:13], v[10:11], off
	ds_read_b128 v[10:13], v25 offset:4096
	ds_read_b128 v[14:17], v24 offset:4096
	s_waitcnt lgkmcnt(1)
	v_mul_f32_e32 v26, v11, v11
	v_mul_f32_e32 v27, v13, v13
	v_fmac_f32_e32 v26, v10, v10
	v_fmac_f32_e32 v27, v12, v12
	v_add_f32_e32 v26, v26, v27
	s_waitcnt lgkmcnt(0)
	v_mul_f32_e32 v27, v15, v15
	v_fmac_f32_e32 v27, v14, v14
	v_add_f32_e32 v26, v26, v27
	v_mul_f32_e32 v27, v17, v17
	v_fmac_f32_e32 v27, v16, v16
	v_add_f32_e32 v26, v27, v26
	s_nop 1
	v_mov_b32_dpp v27, v26 quad_perm:[1,0,3,2] row_mask:0xf bank_mask:0xf
	s_waitcnt lgkmcnt(0)
	v_add_f32_e32 v26, v26, v27
	s_nop 1
	v_mov_b32_dpp v27, v26 quad_perm:[2,3,0,1] row_mask:0xf bank_mask:0xf
	s_waitcnt lgkmcnt(0)
	v_add_f32_e32 v26, v26, v27
	s_nop 1
	v_mov_b32_dpp v27, v26 row_half_mirror row_mask:0xf bank_mask:0xf
	s_waitcnt lgkmcnt(0)
	v_add_f32_e32 v26, v26, v27
	s_nop 1
	v_mov_b32_dpp v27, v26 row_mirror row_mask:0xf bank_mask:0xf
	s_waitcnt lgkmcnt(0)
	v_add_f32_e32 v26, v26, v27
	v_fmamk_f32 v26, v26, 0x3c000000, v232
	v_cmp_gt_f32_e32 vcc, s82, v26
	v_mul_f32_e32 v27, 0x4f800000, v26
	s_nop 0
	v_cndmask_b32_e32 v26, v26, v27, vcc
	v_sqrt_f32_e32 v27, v26
	s_nop 0
	v_add_u32_e32 v28, -1, v27
	v_fma_f32 v29, -v28, v27, v26
	v_cmp_ge_f32_e64 s[44:45], 0, v29
	v_add_u32_e32 v29, 1, v27
	s_nop 0
	v_cndmask_b32_e64 v28, v27, v28, s[44:45]
	v_fma_f32 v27, -v29, v27, v26
	v_cmp_lt_f32_e64 s[44:45], 0, v27
	s_nop 1
	v_cndmask_b32_e64 v27, v28, v29, s[44:45]
	v_mul_f32_e32 v28, 0x37800000, v27
	v_cndmask_b32_e32 v27, v27, v28, vcc
	v_cmp_class_f32_e32 vcc, v26, v229
	s_nop 1
	v_cndmask_b32_e32 v26, v27, v26, vcc
	v_div_scale_f32 v27, s[4:5], v26, v26, v237
	v_rcp_f32_e32 v28, v27
	s_movk_i32 s4, 0x4000
	v_fma_f32 v29, -v27, v28, 1.0
	v_fmac_f32_e32 v28, v29, v28
	v_div_scale_f32 v29, vcc, v237, v26, v237
	v_mul_f32_e32 v30, v29, v28
	v_fma_f32 v31, -v27, v30, v29
	v_fmac_f32_e32 v30, v31, v28
	v_fma_f32 v27, -v27, v30, v29
	v_div_fmas_f32 v27, v27, v28, v30
	v_div_fixup_f32 v26, v27, v26, v237
	v_mul_f32_e32 v10, v10, v26
	v_mul_f32_e32 v11, v11, v26
	v_mul_f32_e32 v10, v6, v10
	v_mul_f32_e32 v11, v7, v11
	v_med3_f32 v10, v10, s33, v233
	v_med3_f32 v11, v11, s33, v233
	v_mov_b32_e32 v27, v1
	v_cvt_pk_fp8_f32 v27, v10, v11
	v_mul_f32_e32 v12, v12, v26
	v_mul_f32_e32 v13, v13, v26
	v_mul_f32_e32 v12, v8, v12
	v_mul_f32_e32 v13, v9, v13
	v_med3_f32 v10, v12, s33, v233
	v_med3_f32 v11, v13, s33, v233
	v_cvt_pk_fp8_f32 v27, v10, v11 op_sel:[0,0,1]
	v_mul_f32_e32 v10, v14, v26
	v_mul_f32_e32 v11, v15, v26
	v_mul_f32_e32 v10, v2, v10
	v_mul_f32_e32 v11, v3, v11
	v_med3_f32 v10, v10, s33, v233
	v_med3_f32 v11, v11, s33, v233
	v_mov_b32_e32 v14, v1
	v_cvt_pk_fp8_f32 v14, v10, v11
	v_mul_f32_e32 v12, v16, v26
	v_mul_f32_e32 v13, v17, v26
	v_mul_f32_e32 v12, v4, v12
	v_mul_f32_e32 v13, v5, v13
	v_med3_f32 v10, v12, s33, v233
	v_med3_f32 v11, v13, s33, v233
	v_cvt_pk_fp8_f32 v14, v10, v11 op_sel:[0,0,1]
	v_add_co_u32_e32 v12, vcc, s4, v18
	v_cndmask_b32_e64 v10, v14, v27, s[42:43]
	v_cndmask_b32_e64 v11, v27, v14, s[42:43]
	v_addc_co_u32_e32 v13, vcc, 0, v19, vcc
	global_store_dwordx2 v[12:13], v[10:11], off
	ds_read_b128 v[10:13], v25 offset:6144
	ds_read_b128 v[14:17], v24 offset:6144
	s_waitcnt lgkmcnt(1)
	v_mul_f32_e32 v26, v11, v11
	v_mul_f32_e32 v27, v13, v13
	v_fmac_f32_e32 v26, v10, v10
	v_fmac_f32_e32 v27, v12, v12
	v_add_f32_e32 v26, v26, v27
	s_waitcnt lgkmcnt(0)
	v_mul_f32_e32 v27, v15, v15
	v_fmac_f32_e32 v27, v14, v14
	v_add_f32_e32 v26, v26, v27
	v_mul_f32_e32 v27, v17, v17
	v_fmac_f32_e32 v27, v16, v16
	v_add_f32_e32 v26, v27, v26
	s_nop 1
	v_mov_b32_dpp v27, v26 quad_perm:[1,0,3,2] row_mask:0xf bank_mask:0xf
	s_waitcnt lgkmcnt(0)
	v_add_f32_e32 v26, v26, v27
	s_nop 1
	v_mov_b32_dpp v27, v26 quad_perm:[2,3,0,1] row_mask:0xf bank_mask:0xf
	s_waitcnt lgkmcnt(0)
	v_add_f32_e32 v26, v26, v27
	s_nop 1
	v_mov_b32_dpp v27, v26 row_half_mirror row_mask:0xf bank_mask:0xf
	s_waitcnt lgkmcnt(0)
	v_add_f32_e32 v26, v26, v27
	s_nop 1
	v_mov_b32_dpp v27, v26 row_mirror row_mask:0xf bank_mask:0xf
	s_waitcnt lgkmcnt(0)
	v_add_f32_e32 v26, v26, v27
	v_fmamk_f32 v26, v26, 0x3c000000, v232
	v_cmp_gt_f32_e32 vcc, s82, v26
	v_mul_f32_e32 v27, 0x4f800000, v26
	s_nop 0
	v_cndmask_b32_e32 v26, v26, v27, vcc
	v_sqrt_f32_e32 v27, v26
	s_nop 0
	v_add_u32_e32 v28, -1, v27
	v_fma_f32 v29, -v28, v27, v26
	v_cmp_ge_f32_e64 s[44:45], 0, v29
	v_add_u32_e32 v29, 1, v27
	s_nop 0
	v_cndmask_b32_e64 v28, v27, v28, s[44:45]
	v_fma_f32 v27, -v29, v27, v26
	v_cmp_lt_f32_e64 s[44:45], 0, v27
	s_nop 1
	v_cndmask_b32_e64 v27, v28, v29, s[44:45]
	v_mul_f32_e32 v28, 0x37800000, v27
	v_cndmask_b32_e32 v27, v27, v28, vcc
	v_cmp_class_f32_e32 vcc, v26, v229
	s_nop 1
	v_cndmask_b32_e32 v26, v27, v26, vcc
	v_div_scale_f32 v27, s[4:5], v26, v26, v237
	v_rcp_f32_e32 v28, v27
	s_movk_i32 s4, 0x6000
	v_fma_f32 v29, -v27, v28, 1.0
	v_fmac_f32_e32 v28, v29, v28
	v_div_scale_f32 v29, vcc, v237, v26, v237
	v_mul_f32_e32 v30, v29, v28
	v_fma_f32 v31, -v27, v30, v29
	v_fmac_f32_e32 v30, v31, v28
	v_fma_f32 v27, -v27, v30, v29
	v_div_fmas_f32 v27, v27, v28, v30
	v_div_fixup_f32 v26, v27, v26, v237
	v_mul_f32_e32 v10, v10, v26
	v_mul_f32_e32 v11, v11, v26
	v_mul_f32_e32 v10, v6, v10
	v_mul_f32_e32 v11, v7, v11
	v_med3_f32 v10, v10, s33, v233
	v_med3_f32 v11, v11, s33, v233
	v_mov_b32_e32 v27, v1
	v_cvt_pk_fp8_f32 v27, v10, v11
	v_mul_f32_e32 v12, v12, v26
	v_mul_f32_e32 v13, v13, v26
	v_mul_f32_e32 v12, v8, v12
	v_mul_f32_e32 v13, v9, v13
	v_med3_f32 v10, v12, s33, v233
	v_med3_f32 v11, v13, s33, v233
	v_cvt_pk_fp8_f32 v27, v10, v11 op_sel:[0,0,1]
	v_mul_f32_e32 v10, v14, v26
	v_mul_f32_e32 v11, v15, v26
	v_mul_f32_e32 v10, v2, v10
	v_mul_f32_e32 v11, v3, v11
	v_med3_f32 v10, v10, s33, v233
	v_med3_f32 v11, v11, s33, v233
	v_mov_b32_e32 v14, v1
	v_cvt_pk_fp8_f32 v14, v10, v11
	v_mul_f32_e32 v12, v16, v26
	v_mul_f32_e32 v13, v17, v26
	v_mul_f32_e32 v12, v4, v12
	v_mul_f32_e32 v13, v5, v13
	v_med3_f32 v10, v12, s33, v233
	v_med3_f32 v11, v13, s33, v233
	v_cvt_pk_fp8_f32 v14, v10, v11 op_sel:[0,0,1]
	v_add_co_u32_e32 v12, vcc, s4, v18
	v_cndmask_b32_e64 v10, v14, v27, s[42:43]
	v_cndmask_b32_e64 v11, v27, v14, s[42:43]
	v_addc_co_u32_e32 v13, vcc, 0, v19, vcc
	global_store_dwordx2 v[12:13], v[10:11], off
	ds_read_b128 v[10:13], v25 offset:8192
	ds_read_b128 v[14:17], v24 offset:8192
	s_waitcnt lgkmcnt(1)
	v_mul_f32_e32 v26, v11, v11
	v_mul_f32_e32 v27, v13, v13
	v_fmac_f32_e32 v26, v10, v10
	v_fmac_f32_e32 v27, v12, v12
	v_add_f32_e32 v26, v26, v27
	s_waitcnt lgkmcnt(0)
	v_mul_f32_e32 v27, v15, v15
	v_fmac_f32_e32 v27, v14, v14
	v_add_f32_e32 v26, v26, v27
	v_mul_f32_e32 v27, v17, v17
	v_fmac_f32_e32 v27, v16, v16
	v_add_f32_e32 v26, v27, v26
	s_nop 1
	v_mov_b32_dpp v27, v26 quad_perm:[1,0,3,2] row_mask:0xf bank_mask:0xf
	s_waitcnt lgkmcnt(0)
	v_add_f32_e32 v26, v26, v27
	s_nop 1
	v_mov_b32_dpp v27, v26 quad_perm:[2,3,0,1] row_mask:0xf bank_mask:0xf
	s_waitcnt lgkmcnt(0)
	v_add_f32_e32 v26, v26, v27
	s_nop 1
	v_mov_b32_dpp v27, v26 row_half_mirror row_mask:0xf bank_mask:0xf
	s_waitcnt lgkmcnt(0)
	v_add_f32_e32 v26, v26, v27
	s_nop 1
	v_mov_b32_dpp v27, v26 row_mirror row_mask:0xf bank_mask:0xf
	s_waitcnt lgkmcnt(0)
	v_add_f32_e32 v26, v26, v27
	v_fmamk_f32 v26, v26, 0x3c000000, v232
	v_cmp_gt_f32_e32 vcc, s82, v26
	v_mul_f32_e32 v27, 0x4f800000, v26
	s_nop 0
	v_cndmask_b32_e32 v26, v26, v27, vcc
	v_sqrt_f32_e32 v27, v26
	s_nop 0
	v_add_u32_e32 v28, -1, v27
	v_fma_f32 v29, -v28, v27, v26
	v_cmp_ge_f32_e64 s[44:45], 0, v29
	v_add_u32_e32 v29, 1, v27
	s_nop 0
	v_cndmask_b32_e64 v28, v27, v28, s[44:45]
	v_fma_f32 v27, -v29, v27, v26
	v_cmp_lt_f32_e64 s[44:45], 0, v27
	s_nop 1
	v_cndmask_b32_e64 v27, v28, v29, s[44:45]
	v_mul_f32_e32 v28, 0x37800000, v27
	v_cndmask_b32_e32 v27, v27, v28, vcc
	v_cmp_class_f32_e32 vcc, v26, v229
	s_nop 1
	v_cndmask_b32_e32 v26, v27, v26, vcc
	v_div_scale_f32 v27, s[4:5], v26, v26, v237
	v_rcp_f32_e32 v28, v27
	s_mov_b32 s4, 0x8000
	v_fma_f32 v29, -v27, v28, 1.0
	v_fmac_f32_e32 v28, v29, v28
	v_div_scale_f32 v29, vcc, v237, v26, v237
	v_mul_f32_e32 v30, v29, v28
	v_fma_f32 v31, -v27, v30, v29
	v_fmac_f32_e32 v30, v31, v28
	v_fma_f32 v27, -v27, v30, v29
	v_div_fmas_f32 v27, v27, v28, v30
	v_div_fixup_f32 v26, v27, v26, v237
	v_mul_f32_e32 v10, v10, v26
	v_mul_f32_e32 v11, v11, v26
	v_mul_f32_e32 v10, v6, v10
	v_mul_f32_e32 v11, v7, v11
	v_med3_f32 v10, v10, s33, v233
	v_med3_f32 v11, v11, s33, v233
	v_mov_b32_e32 v27, v1
	v_cvt_pk_fp8_f32 v27, v10, v11
	v_mul_f32_e32 v12, v12, v26
	v_mul_f32_e32 v13, v13, v26
	v_mul_f32_e32 v12, v8, v12
	v_mul_f32_e32 v13, v9, v13
	v_med3_f32 v10, v12, s33, v233
	v_med3_f32 v11, v13, s33, v233
	v_cvt_pk_fp8_f32 v27, v10, v11 op_sel:[0,0,1]
	v_mul_f32_e32 v10, v14, v26
	v_mul_f32_e32 v11, v15, v26
	v_mul_f32_e32 v10, v2, v10
	v_mul_f32_e32 v11, v3, v11
	v_med3_f32 v10, v10, s33, v233
	v_med3_f32 v11, v11, s33, v233
	v_mov_b32_e32 v14, v1
	v_cvt_pk_fp8_f32 v14, v10, v11
	v_mul_f32_e32 v12, v16, v26
	v_mul_f32_e32 v13, v17, v26
	v_mul_f32_e32 v12, v4, v12
	v_mul_f32_e32 v13, v5, v13
	v_med3_f32 v10, v12, s33, v233
	v_med3_f32 v11, v13, s33, v233
	v_cvt_pk_fp8_f32 v14, v10, v11 op_sel:[0,0,1]
	v_add_co_u32_e32 v12, vcc, s4, v18
	v_cndmask_b32_e64 v10, v14, v27, s[42:43]
	v_cndmask_b32_e64 v11, v27, v14, s[42:43]
	v_addc_co_u32_e32 v13, vcc, 0, v19, vcc
	global_store_dwordx2 v[12:13], v[10:11], off
	ds_read_b128 v[10:13], v25 offset:10240
	ds_read_b128 v[14:17], v24 offset:10240
	s_waitcnt lgkmcnt(1)
	v_mul_f32_e32 v26, v11, v11
	v_mul_f32_e32 v27, v13, v13
	v_fmac_f32_e32 v26, v10, v10
	v_fmac_f32_e32 v27, v12, v12
	v_add_f32_e32 v26, v26, v27
	s_waitcnt lgkmcnt(0)
	v_mul_f32_e32 v27, v15, v15
	v_fmac_f32_e32 v27, v14, v14
	v_add_f32_e32 v26, v26, v27
	v_mul_f32_e32 v27, v17, v17
	v_fmac_f32_e32 v27, v16, v16
	v_add_f32_e32 v26, v27, v26
	s_nop 1
	v_mov_b32_dpp v27, v26 quad_perm:[1,0,3,2] row_mask:0xf bank_mask:0xf
	s_waitcnt lgkmcnt(0)
	v_add_f32_e32 v26, v26, v27
	s_nop 1
	v_mov_b32_dpp v27, v26 quad_perm:[2,3,0,1] row_mask:0xf bank_mask:0xf
	s_waitcnt lgkmcnt(0)
	v_add_f32_e32 v26, v26, v27
	s_nop 1
	v_mov_b32_dpp v27, v26 row_half_mirror row_mask:0xf bank_mask:0xf
	s_waitcnt lgkmcnt(0)
	v_add_f32_e32 v26, v26, v27
	s_nop 1
	v_mov_b32_dpp v27, v26 row_mirror row_mask:0xf bank_mask:0xf
	s_waitcnt lgkmcnt(0)
	v_add_f32_e32 v26, v26, v27
	v_fmamk_f32 v26, v26, 0x3c000000, v232
	v_cmp_gt_f32_e32 vcc, s82, v26
	v_mul_f32_e32 v27, 0x4f800000, v26
	s_nop 0
	v_cndmask_b32_e32 v26, v26, v27, vcc
	v_sqrt_f32_e32 v27, v26
	s_nop 0
	v_add_u32_e32 v28, -1, v27
	v_fma_f32 v29, -v28, v27, v26
	v_cmp_ge_f32_e64 s[44:45], 0, v29
	v_add_u32_e32 v29, 1, v27
	s_nop 0
	v_cndmask_b32_e64 v28, v27, v28, s[44:45]
	v_fma_f32 v27, -v29, v27, v26
	v_cmp_lt_f32_e64 s[44:45], 0, v27
	s_nop 1
	v_cndmask_b32_e64 v27, v28, v29, s[44:45]
	v_mul_f32_e32 v28, 0x37800000, v27
	v_cndmask_b32_e32 v27, v27, v28, vcc
	v_cmp_class_f32_e32 vcc, v26, v229
	s_nop 1
	v_cndmask_b32_e32 v26, v27, v26, vcc
	v_div_scale_f32 v27, s[4:5], v26, v26, v237
	v_rcp_f32_e32 v28, v27
	s_mov_b32 s4, 0xa000
	v_fma_f32 v29, -v27, v28, 1.0
	v_fmac_f32_e32 v28, v29, v28
	v_div_scale_f32 v29, vcc, v237, v26, v237
	v_mul_f32_e32 v30, v29, v28
	v_fma_f32 v31, -v27, v30, v29
	v_fmac_f32_e32 v30, v31, v28
	v_fma_f32 v27, -v27, v30, v29
	v_div_fmas_f32 v27, v27, v28, v30
	v_div_fixup_f32 v26, v27, v26, v237
	v_mul_f32_e32 v10, v10, v26
	v_mul_f32_e32 v11, v11, v26
	v_mul_f32_e32 v10, v6, v10
	v_mul_f32_e32 v11, v7, v11
	v_med3_f32 v10, v10, s33, v233
	v_med3_f32 v11, v11, s33, v233
	v_mov_b32_e32 v27, v1
	v_cvt_pk_fp8_f32 v27, v10, v11
	v_mul_f32_e32 v12, v12, v26
	v_mul_f32_e32 v13, v13, v26
	v_mul_f32_e32 v12, v8, v12
	v_mul_f32_e32 v13, v9, v13
	v_med3_f32 v10, v12, s33, v233
	v_med3_f32 v11, v13, s33, v233
	v_cvt_pk_fp8_f32 v27, v10, v11 op_sel:[0,0,1]
	v_mul_f32_e32 v10, v14, v26
	v_mul_f32_e32 v11, v15, v26
	v_mul_f32_e32 v10, v2, v10
	v_mul_f32_e32 v11, v3, v11
	v_med3_f32 v10, v10, s33, v233
	v_med3_f32 v11, v11, s33, v233
	v_mov_b32_e32 v14, v1
	v_cvt_pk_fp8_f32 v14, v10, v11
	v_mul_f32_e32 v12, v16, v26
	v_mul_f32_e32 v13, v17, v26
	v_mul_f32_e32 v12, v4, v12
	v_mul_f32_e32 v13, v5, v13
	v_med3_f32 v10, v12, s33, v233
	v_med3_f32 v11, v13, s33, v233
	v_cvt_pk_fp8_f32 v14, v10, v11 op_sel:[0,0,1]
	v_add_co_u32_e32 v12, vcc, s4, v18
	v_cndmask_b32_e64 v10, v14, v27, s[42:43]
	v_cndmask_b32_e64 v11, v27, v14, s[42:43]
	v_addc_co_u32_e32 v13, vcc, 0, v19, vcc
	global_store_dwordx2 v[12:13], v[10:11], off
	ds_read_b128 v[10:13], v25 offset:12288
	ds_read_b128 v[14:17], v24 offset:12288
	s_waitcnt lgkmcnt(1)
	v_mul_f32_e32 v26, v11, v11
	v_mul_f32_e32 v27, v13, v13
	v_fmac_f32_e32 v26, v10, v10
	v_fmac_f32_e32 v27, v12, v12
	v_add_f32_e32 v26, v26, v27
	s_waitcnt lgkmcnt(0)
	v_mul_f32_e32 v27, v15, v15
	v_fmac_f32_e32 v27, v14, v14
	v_add_f32_e32 v26, v26, v27
	v_mul_f32_e32 v27, v17, v17
	v_fmac_f32_e32 v27, v16, v16
	v_add_f32_e32 v26, v27, v26
	s_nop 1
	v_mov_b32_dpp v27, v26 quad_perm:[1,0,3,2] row_mask:0xf bank_mask:0xf
	s_waitcnt lgkmcnt(0)
	v_add_f32_e32 v26, v26, v27
	s_nop 1
	v_mov_b32_dpp v27, v26 quad_perm:[2,3,0,1] row_mask:0xf bank_mask:0xf
	s_waitcnt lgkmcnt(0)
	v_add_f32_e32 v26, v26, v27
	s_nop 1
	v_mov_b32_dpp v27, v26 row_half_mirror row_mask:0xf bank_mask:0xf
	s_waitcnt lgkmcnt(0)
	v_add_f32_e32 v26, v26, v27
	s_nop 1
	v_mov_b32_dpp v27, v26 row_mirror row_mask:0xf bank_mask:0xf
	s_waitcnt lgkmcnt(0)
	v_add_f32_e32 v26, v26, v27
	v_fmamk_f32 v26, v26, 0x3c000000, v232
	v_cmp_gt_f32_e32 vcc, s82, v26
	v_mul_f32_e32 v27, 0x4f800000, v26
	s_nop 0
	v_cndmask_b32_e32 v26, v26, v27, vcc
	v_sqrt_f32_e32 v27, v26
	s_nop 0
	v_add_u32_e32 v28, -1, v27
	v_fma_f32 v29, -v28, v27, v26
	v_cmp_ge_f32_e64 s[44:45], 0, v29
	v_add_u32_e32 v29, 1, v27
	s_nop 0
	v_cndmask_b32_e64 v28, v27, v28, s[44:45]
	v_fma_f32 v27, -v29, v27, v26
	v_cmp_lt_f32_e64 s[44:45], 0, v27
	s_nop 1
	v_cndmask_b32_e64 v27, v28, v29, s[44:45]
	v_mul_f32_e32 v28, 0x37800000, v27
	v_cndmask_b32_e32 v27, v27, v28, vcc
	v_cmp_class_f32_e32 vcc, v26, v229
	s_nop 1
	v_cndmask_b32_e32 v26, v27, v26, vcc
	v_div_scale_f32 v27, s[4:5], v26, v26, v237
	v_rcp_f32_e32 v28, v27
	s_mov_b32 s4, 0xc000
	v_fma_f32 v29, -v27, v28, 1.0
	v_fmac_f32_e32 v28, v29, v28
	v_div_scale_f32 v29, vcc, v237, v26, v237
	v_mul_f32_e32 v30, v29, v28
	v_fma_f32 v31, -v27, v30, v29
	v_fmac_f32_e32 v30, v31, v28
	v_fma_f32 v27, -v27, v30, v29
	v_div_fmas_f32 v27, v27, v28, v30
	v_div_fixup_f32 v26, v27, v26, v237
	v_mul_f32_e32 v10, v10, v26
	v_mul_f32_e32 v11, v11, v26
	v_mul_f32_e32 v10, v6, v10
	v_mul_f32_e32 v11, v7, v11
	v_med3_f32 v10, v10, s33, v233
	v_med3_f32 v11, v11, s33, v233
	v_mov_b32_e32 v27, v1
	v_cvt_pk_fp8_f32 v27, v10, v11
	v_mul_f32_e32 v12, v12, v26
	v_mul_f32_e32 v13, v13, v26
	v_mul_f32_e32 v12, v8, v12
	v_mul_f32_e32 v13, v9, v13
	v_med3_f32 v10, v12, s33, v233
	v_med3_f32 v11, v13, s33, v233
	v_cvt_pk_fp8_f32 v27, v10, v11 op_sel:[0,0,1]
	v_mul_f32_e32 v10, v14, v26
	v_mul_f32_e32 v11, v15, v26
	v_mul_f32_e32 v10, v2, v10
	v_mul_f32_e32 v11, v3, v11
	v_med3_f32 v10, v10, s33, v233
	v_med3_f32 v11, v11, s33, v233
	v_mov_b32_e32 v14, v1
	v_cvt_pk_fp8_f32 v14, v10, v11
	v_mul_f32_e32 v12, v16, v26
	v_mul_f32_e32 v13, v17, v26
	v_mul_f32_e32 v12, v4, v12
	v_mul_f32_e32 v13, v5, v13
	v_med3_f32 v10, v12, s33, v233
	v_med3_f32 v11, v13, s33, v233
	v_cvt_pk_fp8_f32 v14, v10, v11 op_sel:[0,0,1]
	v_add_co_u32_e32 v12, vcc, s4, v18
	v_cndmask_b32_e64 v10, v14, v27, s[42:43]
	v_cndmask_b32_e64 v11, v27, v14, s[42:43]
	v_addc_co_u32_e32 v13, vcc, 0, v19, vcc
	global_store_dwordx2 v[12:13], v[10:11], off
	ds_read_b128 v[14:17], v25 offset:14336
	ds_read_b128 v[10:13], v24 offset:14336
	s_waitcnt lgkmcnt(1)
	v_mul_f32_e32 v24, v15, v15
	v_mul_f32_e32 v25, v17, v17
	v_fmac_f32_e32 v24, v14, v14
	v_fmac_f32_e32 v25, v16, v16
	v_add_f32_e32 v24, v24, v25
	s_waitcnt lgkmcnt(0)
	v_mul_f32_e32 v25, v11, v11
	v_fmac_f32_e32 v25, v10, v10
	v_add_f32_e32 v24, v24, v25
	v_mul_f32_e32 v25, v13, v13
	v_fmac_f32_e32 v25, v12, v12
	v_add_f32_e32 v24, v25, v24
	s_nop 1
	v_mov_b32_dpp v23, v24 quad_perm:[1,0,3,2] row_mask:0xf bank_mask:0xf
	s_waitcnt lgkmcnt(0)
	v_add_f32_e32 v23, v24, v23
	s_nop 1
	v_mov_b32_dpp v22, v23 quad_perm:[2,3,0,1] row_mask:0xf bank_mask:0xf
	s_waitcnt lgkmcnt(0)
	v_add_f32_e32 v22, v23, v22
	s_nop 1
	v_mov_b32_dpp v21, v22 row_half_mirror row_mask:0xf bank_mask:0xf
	s_waitcnt lgkmcnt(0)
	v_add_f32_e32 v21, v22, v21
	s_nop 1
	v_mov_b32_dpp v20, v21 row_mirror row_mask:0xf bank_mask:0xf
	s_waitcnt lgkmcnt(0)
	v_add_f32_e32 v20, v21, v20
	v_fmamk_f32 v20, v20, 0x3c000000, v232
	v_cmp_gt_f32_e32 vcc, s82, v20
	v_mul_f32_e32 v21, 0x4f800000, v20
	s_nop 0
	v_cndmask_b32_e32 v20, v20, v21, vcc
	v_sqrt_f32_e32 v21, v20
	s_nop 0
	v_add_u32_e32 v22, -1, v21
	v_fma_f32 v23, -v22, v21, v20
	v_cmp_ge_f32_e64 s[44:45], 0, v23
	v_add_u32_e32 v23, 1, v21
	s_nop 0
	v_cndmask_b32_e64 v22, v21, v22, s[44:45]
	v_fma_f32 v21, -v23, v21, v20
	v_cmp_lt_f32_e64 s[44:45], 0, v21
	s_nop 1
	v_cndmask_b32_e64 v21, v22, v23, s[44:45]
	v_mul_f32_e32 v22, 0x37800000, v21
	v_cndmask_b32_e32 v21, v21, v22, vcc
	v_cmp_class_f32_e32 vcc, v20, v229
	s_nop 1
	v_cndmask_b32_e32 v20, v21, v20, vcc
	v_div_scale_f32 v21, s[4:5], v20, v20, v237
	v_rcp_f32_e32 v22, v21
	s_nop 0
	v_fma_f32 v23, -v21, v22, 1.0
	v_fmac_f32_e32 v22, v23, v22
	v_div_scale_f32 v23, vcc, v237, v20, v237
	v_mul_f32_e32 v24, v23, v22
	v_fma_f32 v25, -v21, v24, v23
	v_fmac_f32_e32 v24, v25, v22
	v_fma_f32 v21, -v21, v24, v23
	v_div_fmas_f32 v21, v21, v22, v24
	v_div_fixup_f32 v20, v21, v20, v237
	v_mul_f32_e32 v14, v14, v20
	v_mul_f32_e32 v6, v6, v14
	v_mul_f32_e32 v14, v15, v20
	v_mul_f32_e32 v7, v7, v14
	v_mul_f32_e32 v14, v16, v20
	v_mul_f32_e32 v8, v8, v14
	v_mul_f32_e32 v14, v17, v20
	v_mul_f32_e32 v9, v9, v14
	v_med3_f32 v6, v6, s33, v233
	v_med3_f32 v7, v7, s33, v233
	v_mov_b32_e32 v14, v1
	v_cvt_pk_fp8_f32 v14, v6, v7
	v_med3_f32 v6, v8, s33, v233
	v_med3_f32 v7, v9, s33, v233
	v_cvt_pk_fp8_f32 v14, v6, v7 op_sel:[0,0,1]
	v_mul_f32_e32 v6, v10, v20
	v_mul_f32_e32 v2, v2, v6
	v_mul_f32_e32 v6, v11, v20
	v_mul_f32_e32 v3, v3, v6
	v_mul_f32_e32 v6, v12, v20
	v_mul_f32_e32 v4, v4, v6
	v_mul_f32_e32 v6, v13, v20
	v_mul_f32_e32 v5, v5, v6
	v_med3_f32 v2, v2, s33, v233
	v_med3_f32 v3, v3, s33, v233
	v_mov_b32_e32 v6, v1
	v_cvt_pk_fp8_f32 v6, v2, v3
	v_med3_f32 v2, v4, s33, v233
	v_med3_f32 v3, v5, s33, v233
	v_add_co_u32_e32 v4, vcc, 0xe000, v18
	v_cvt_pk_fp8_f32 v6, v2, v3 op_sel:[0,0,1]
	s_nop 0
	v_addc_co_u32_e32 v5, vcc, 0, v19, vcc
	v_cndmask_b32_e64 v2, v6, v14, s[42:43]
	v_cndmask_b32_e64 v3, v14, v6, s[42:43]
	global_store_dwordx2 v[4:5], v[2:3], off
	s_branch .LBB0_1020
